# strategy 2 (prologue de-serialisation): combine block prologue issues the token-table loads with the parameter loads; dead zero-inits before fp8 pack pairs removed in the G4/G5 epilogues
# speedup vs baseline: 1.0050x; 1.0050x over previous
; DI float kf(float c) { asm volatile("" : "+v"(c)); return c; }
; DI unsigned pk_fp8x4(float a, float b, float c, float d) { int p = 0; p = __builtin_amdgcn_cvt_pk_fp8_f32(a, b, p, false); p = __builtin_amdgcn_cvt_pk_fp8_f32(c, d, p, true); return (unsigned)p; }
;     DI void operator()(const f32x4 (&acc)[2][2][4][2], const Unit& u, int wr, int wc, int fr, int fq) const {
;         const int row0 = u.pm * BM + wr * 64 + fr + (fq & 1) * 16; const int col0 = u.pn * HALF + wc * 32 + 8 * (fq & ~1); const float c7 = kf(7.f);
; #pragma unroll
;         for (int ai = 0; ai < 2; ++ai)
; #pragma unroll
;             for (int mp = 0; mp < 2; ++mp) { unsigned char* rowp = O + (size_t)(row0 + ai * HALF + mp * 32) * ldc + col0;
;                 u32x2 w[2];
; #pragma unroll
;                 for (int mm = 0; mm < 2; ++mm) { const int m = 2 * mp + mm; float o[8];
; #pragma unroll
;                     for (int n = 0; n < 2; ++n) { const f32x4 g = acc[ai][0][m][n], l = acc[ai][1][m][n];
; #pragma unroll
;                         for (int jp = 0; jp < 2; ++jp) {
;                             const f32x2 xg = __builtin_elementwise_min((f32x2){g[2 * jp], g[2 * jp + 1]}, (f32x2){c7, c7});
;                             const f32x2 xl = __builtin_elementwise_min(__builtin_elementwise_max((f32x2){l[2 * jp], l[2 * jp + 1]}, (f32x2){-c7, -c7}), (f32x2){c7, c7});
;                             const f32x2 z = xg * (-1.702f * 1.44269504f); f32x2 e; e.x = __builtin_amdgcn_exp2f(z.x); e.y = __builtin_amdgcn_exp2f(z.y);
;                             const f32x2 dn = e + 1.f; f32x2 rc; rc.x = __builtin_amdgcn_rcpf(dn.x); rc.y = __builtin_amdgcn_rcpf(dn.y);
;                             const f32x2 r2 = (xg * rc) * (xl + 1.f); o[n * 4 + 2 * jp] = r2.x; o[n * 4 + 2 * jp + 1] = r2.y; } }
;                     w[mm].x = pk_fp8x4(o[0], o[1], o[2], o[3]); w[mm].y = pk_fp8x4(o[4], o[5], o[6], o[7]); }
;                 const u32x2 sx = __builtin_amdgcn_permlane16_swap(w[0].x, w[1].x, false, false), sy = __builtin_amdgcn_permlane16_swap(w[0].y, w[1].y, false, false);
;                 *(u32x4*)rowp = (u32x4){sx.x, sy.x, sx.y, sy.y}; }
.LBB0_1192:
	s_lshl_b32 s2, s82, 8
	v_mbcnt_lo_u32_b32 v0, -1, 0
	v_mbcnt_hi_u32_b32 v0, -1, v0
	s_add_i32 s2, s2, s90
	v_and_or_b32 v4, v0, 31, s2
	s_lshl_b32 s2, s10, 7
	v_ashrrev_i32_e32 v0, 1, v0
	s_or_b32 s2, s2, s72
	v_and_b32_e32 v0, -16, v0
	v_mov_b32_e32 v7, 0x40e00000
	v_ashrrev_i32_e32 v5, 31, v4
	v_add_u32_e32 v2, s2, v0
	v_lshlrev_b64 v[0:1], 10, v[4:5]
	v_max_f32_e32 v6, v7, v7
	v_min_f32_e32 v9, v189, v6
	v_min_f32_e32 v8, v188, v6
	v_pk_mul_f32 v[10:11], v[8:9], s[84:85] op_sel_hi:[1,0]
	v_max_f32_e64 v7, -v7, -v7
	v_exp_f32_e32 v10, v10
	v_exp_f32_e32 v11, v11
	s_nop 0
	v_pk_add_f32 v[10:11], v[10:11], 1.0 op_sel_hi:[1,0]
	v_rcp_f32_e32 v10, v10
	v_rcp_f32_e32 v11, v11
	v_med3_f32 v13, v185, v7, v6
	v_med3_f32 v12, v184, v7, v6
	v_pk_mul_f32 v[8:9], v[8:9], v[10:11]
	v_pk_add_f32 v[10:11], v[12:13], 1.0 op_sel_hi:[1,0]
	v_pk_mul_f32 v[10:11], v[10:11], v[8:9]
	v_min_f32_e32 v9, v191, v6
	v_min_f32_e32 v8, v190, v6
	v_pk_mul_f32 v[12:13], v[8:9], s[84:85] op_sel_hi:[1,0]
	v_exp_f32_e32 v12, v12
	v_exp_f32_e32 v13, v13
	v_med3_f32 v15, v187, v7, v6
	v_pk_add_f32 v[12:13], v[12:13], 1.0 op_sel_hi:[1,0]
	v_med3_f32 v14, v186, v7, v6
	v_rcp_f32_e32 v12, v12
	v_rcp_f32_e32 v13, v13
	s_nop 0
	v_pk_mul_f32 v[8:9], v[8:9], v[12:13]
	v_pk_add_f32 v[12:13], v[14:15], 1.0 op_sel_hi:[1,0]
	v_med3_f32 v17, v177, v7, v6
	v_pk_mul_f32 v[12:13], v[12:13], v[8:9]
	v_min_f32_e32 v9, v181, v6
	v_min_f32_e32 v8, v180, v6
	v_pk_mul_f32 v[14:15], v[8:9], s[84:85] op_sel_hi:[1,0]
	v_exp_f32_e32 v14, v14
	v_exp_f32_e32 v15, v15
	v_med3_f32 v16, v176, v7, v6
	v_pk_add_f32 v[14:15], v[14:15], 1.0 op_sel_hi:[1,0]
	v_rcp_f32_e32 v14, v14
	v_rcp_f32_e32 v15, v15
	v_med3_f32 v19, v179, v7, v6
	v_pk_mul_f32 v[8:9], v[8:9], v[14:15]
	v_pk_add_f32 v[14:15], v[16:17], 1.0 op_sel_hi:[1,0]
	v_pk_mul_f32 v[14:15], v[14:15], v[8:9]
	v_min_f32_e32 v9, v183, v6
	v_min_f32_e32 v8, v182, v6
	v_pk_mul_f32 v[16:17], v[8:9], s[84:85] op_sel_hi:[1,0]
	v_exp_f32_e32 v16, v16
	v_exp_f32_e32 v17, v17
	v_med3_f32 v18, v178, v7, v6
	v_pk_add_f32 v[16:17], v[16:17], 1.0 op_sel_hi:[1,0]
	v_med3_f32 v21, v163, v7, v6
	v_rcp_f32_e32 v16, v16
	v_rcp_f32_e32 v17, v17
	v_ashrrev_i32_e32 v3, 31, v2
	v_lshl_add_u64 v[0:1], s[46:47], 0, v[0:1]
	v_lshl_add_u64 v[0:1], v[0:1], 0, v[2:3]
	v_pk_mul_f32 v[16:17], v[8:9], v[16:17]
	v_cvt_pk_fp8_f32 v9, v14, v15
	v_cvt_pk_fp8_f32 v8, v10, v11
	v_pk_add_f32 v[10:11], v[18:19], 1.0 op_sel_hi:[1,0]
	v_pk_mul_f32 v[10:11], v[10:11], v[16:17]
	v_cvt_pk_fp8_f32 v8, v12, v13 op_sel:[0,0,1]
	v_cvt_pk_fp8_f32 v9, v10, v11 op_sel:[0,0,1]
	v_min_f32_e32 v11, v173, v6
	v_min_f32_e32 v10, v172, v6
	v_pk_mul_f32 v[12:13], v[10:11], s[84:85] op_sel_hi:[1,0]
	v_exp_f32_e32 v12, v12
	v_exp_f32_e32 v13, v13
	v_med3_f32 v15, v169, v7, v6
	v_pk_add_f32 v[12:13], v[12:13], 1.0 op_sel_hi:[1,0]
	v_med3_f32 v14, v168, v7, v6
	v_rcp_f32_e32 v12, v12
	v_rcp_f32_e32 v13, v13
	s_nop 0
	v_pk_mul_f32 v[10:11], v[10:11], v[12:13]
	v_pk_add_f32 v[12:13], v[14:15], 1.0 op_sel_hi:[1,0]
	v_med3_f32 v17, v171, v7, v6
	v_pk_mul_f32 v[12:13], v[12:13], v[10:11]
	v_min_f32_e32 v11, v175, v6
	v_min_f32_e32 v10, v174, v6
	v_pk_mul_f32 v[14:15], v[10:11], s[84:85] op_sel_hi:[1,0]
	v_exp_f32_e32 v14, v14
	v_exp_f32_e32 v15, v15
	v_med3_f32 v16, v170, v7, v6
	v_pk_add_f32 v[14:15], v[14:15], 1.0 op_sel_hi:[1,0]
	v_rcp_f32_e32 v14, v14
	v_rcp_f32_e32 v15, v15
	v_med3_f32 v19, v161, v7, v6
	v_or_b32_e32 v4, 32, v4
	v_pk_mul_f32 v[10:11], v[10:11], v[14:15]
	v_pk_add_f32 v[14:15], v[16:17], 1.0 op_sel_hi:[1,0]
	s_mov_b32 s2, 0x20000
	v_pk_mul_f32 v[14:15], v[14:15], v[10:11]
	v_min_f32_e32 v11, v165, v6
	v_min_f32_e32 v10, v164, v6
	v_pk_mul_f32 v[16:17], v[10:11], s[84:85] op_sel_hi:[1,0]
	v_exp_f32_e32 v16, v16
	v_exp_f32_e32 v17, v17
	v_med3_f32 v18, v160, v7, v6
	v_pk_add_f32 v[16:17], v[16:17], 1.0 op_sel_hi:[1,0]
	s_mov_b64 s[4:5], -1
	v_rcp_f32_e32 v16, v16
	v_rcp_f32_e32 v17, v17
	s_nop 0
	v_pk_mul_f32 v[10:11], v[10:11], v[16:17]
	v_pk_add_f32 v[16:17], v[18:19], 1.0 op_sel_hi:[1,0]
	s_nop 0
	v_pk_mul_f32 v[16:17], v[16:17], v[10:11]
	v_min_f32_e32 v11, v167, v6
	v_min_f32_e32 v10, v166, v6
	v_pk_mul_f32 v[18:19], v[10:11], s[84:85] op_sel_hi:[1,0]
	v_exp_f32_e32 v18, v18
	v_exp_f32_e32 v19, v19
	v_med3_f32 v20, v162, v7, v6
	v_ashrrev_i32_e32 v5, 31, v4
	v_pk_add_f32 v[18:19], v[18:19], 1.0 op_sel_hi:[1,0]
	v_lshlrev_b64 v[4:5], 10, v[4:5]
	v_rcp_f32_e32 v18, v18
	v_rcp_f32_e32 v19, v19
	v_lshl_add_u64 v[4:5], s[46:47], 0, v[4:5]
	v_lshl_add_u64 v[2:3], v[4:5], 0, v[2:3]
	v_pk_mul_f32 v[18:19], v[10:11], v[18:19]
	v_cvt_pk_fp8_f32 v10, v12, v13
	v_cvt_pk_fp8_f32 v11, v16, v17
	v_pk_add_f32 v[12:13], v[20:21], 1.0 op_sel_hi:[1,0]
	v_pk_mul_f32 v[12:13], v[12:13], v[18:19]
	v_cvt_pk_fp8_f32 v10, v14, v15 op_sel:[0,0,1]
	v_cvt_pk_fp8_f32 v11, v12, v13 op_sel:[0,0,1]
	s_nop 0
	v_permlane16_swap_b32_e32 v8, v10
	s_nop 0
	v_permlane16_swap_b32_e32 v9, v11
	global_store_dwordx4 v[0:1], v[8:11], off
	s_nop 1
	v_min_f32_e32 v9, v157, v6
	v_min_f32_e32 v8, v156, v6
	v_pk_mul_f32 v[10:11], v[8:9], s[84:85] op_sel_hi:[1,0]
	v_med3_f32 v13, v153, v7, v6
	v_exp_f32_e32 v10, v10
	v_exp_f32_e32 v11, v11
	v_med3_f32 v12, v152, v7, v6
	v_pk_add_f32 v[10:11], v[10:11], 1.0 op_sel_hi:[1,0]
	v_rcp_f32_e32 v10, v10
	v_rcp_f32_e32 v11, v11
	v_med3_f32 v15, v155, v7, v6
	v_med3_f32 v14, v154, v7, v6
	v_pk_mul_f32 v[8:9], v[8:9], v[10:11]
	v_pk_add_f32 v[10:11], v[12:13], 1.0 op_sel_hi:[1,0]
	v_pk_mul_f32 v[10:11], v[10:11], v[8:9]
	v_min_f32_e32 v9, v159, v6
	v_min_f32_e32 v8, v158, v6
	v_pk_mul_f32 v[12:13], v[8:9], s[84:85] op_sel_hi:[1,0]
	v_exp_f32_e32 v12, v12
	v_exp_f32_e32 v13, v13
; DI float kf(float c) { asm volatile("" : "+v"(c)); return c; }
; DI unsigned pk_fp8x4(float a, float b, float c, float d) { int p = 0; p = __builtin_amdgcn_cvt_pk_fp8_f32(a, b, p, false); p = __builtin_amdgcn_cvt_pk_fp8_f32(c, d, p, true); return (unsigned)p; }
;     DI void operator()(const f32x4 (&acc)[2][2][4][2], const Unit& u, int wr, int wc, int fr, int fq) const {
;         const int row0 = u.pm * BM + wr * 64 + fr + (fq & 1) * 16; const int col0 = u.pn * HALF + wc * 32 + 8 * (fq & ~1); const float c7 = kf(7.f);
; #pragma unroll
;         for (int ai = 0; ai < 2; ++ai)
; #pragma unroll
;             for (int mp = 0; mp < 2; ++mp) { unsigned char* rowp = O + (size_t)(row0 + ai * HALF + mp * 32) * ldc + col0;
;                 u32x2 w[2];
; #pragma unroll
;                 for (int mm = 0; mm < 2; ++mm) { const int m = 2 * mp + mm; float o[8];
; #pragma unroll
;                     for (int n = 0; n < 2; ++n) { const f32x4 g = acc[ai][0][m][n], l = acc[ai][1][m][n];
; #pragma unroll
;                         for (int jp = 0; jp < 2; ++jp) {
;                             const f32x2 xg = __builtin_elementwise_min((f32x2){g[2 * jp], g[2 * jp + 1]}, (f32x2){c7, c7});
;                             const f32x2 xl = __builtin_elementwise_min(__builtin_elementwise_max((f32x2){l[2 * jp], l[2 * jp + 1]}, (f32x2){-c7, -c7}), (f32x2){c7, c7});
;                             const f32x2 z = xg * (-1.702f * 1.44269504f); f32x2 e; e.x = __builtin_amdgcn_exp2f(z.x); e.y = __builtin_amdgcn_exp2f(z.y);
;                             const f32x2 dn = e + 1.f; f32x2 rc; rc.x = __builtin_amdgcn_rcpf(dn.x); rc.y = __builtin_amdgcn_rcpf(dn.y);
;                             const f32x2 r2 = (xg * rc) * (xl + 1.f); o[n * 4 + 2 * jp] = r2.x; o[n * 4 + 2 * jp + 1] = r2.y; } }
;                     w[mm].x = pk_fp8x4(o[0], o[1], o[2], o[3]); w[mm].y = pk_fp8x4(o[4], o[5], o[6], o[7]); }
;                 const u32x2 sx = __builtin_amdgcn_permlane16_swap(w[0].x, w[1].x, false, false), sy = __builtin_amdgcn_permlane16_swap(w[0].y, w[1].y, false, false);
;                 *(u32x4*)rowp = (u32x4){sx.x, sy.x, sx.y, sy.y}; }
	v_med3_f32 v17, v145, v7, v6
	v_med3_f32 v16, v144, v7, v6
	v_pk_add_f32 v[12:13], v[12:13], 1.0 op_sel_hi:[1,0]
	v_rcp_f32_e32 v12, v12
	v_rcp_f32_e32 v13, v13
	s_nop 0
	v_pk_mul_f32 v[8:9], v[8:9], v[12:13]
	v_pk_add_f32 v[12:13], v[14:15], 1.0 op_sel_hi:[1,0]
	v_med3_f32 v19, v147, v7, v6
	v_pk_mul_f32 v[12:13], v[12:13], v[8:9]
	v_min_f32_e32 v9, v149, v6
	v_min_f32_e32 v8, v148, v6
	v_pk_mul_f32 v[14:15], v[8:9], s[84:85] op_sel_hi:[1,0]
	v_med3_f32 v18, v146, v7, v6
	v_exp_f32_e32 v14, v14
	v_exp_f32_e32 v15, v15
	s_nop 0
	v_pk_add_f32 v[14:15], v[14:15], 1.0 op_sel_hi:[1,0]
	v_rcp_f32_e32 v14, v14
	v_rcp_f32_e32 v15, v15
	v_med3_f32 v21, v131, v7, v6
	v_med3_f32 v20, v130, v7, v6
	v_pk_mul_f32 v[8:9], v[8:9], v[14:15]
	v_pk_add_f32 v[14:15], v[16:17], 1.0 op_sel_hi:[1,0]
	s_nop 0
	v_pk_mul_f32 v[14:15], v[14:15], v[8:9]
	v_min_f32_e32 v9, v151, v6
	v_min_f32_e32 v8, v150, v6
	v_pk_mul_f32 v[16:17], v[8:9], s[84:85] op_sel_hi:[1,0]
	s_nop 0
	v_exp_f32_e32 v16, v16
	v_exp_f32_e32 v17, v17
	s_nop 0
	v_pk_add_f32 v[16:17], v[16:17], 1.0 op_sel_hi:[1,0]
	s_nop 0
	v_rcp_f32_e32 v16, v16
	v_rcp_f32_e32 v17, v17
	s_nop 0
	v_pk_mul_f32 v[16:17], v[8:9], v[16:17]
	v_cvt_pk_fp8_f32 v9, v14, v15
	v_cvt_pk_fp8_f32 v8, v10, v11
	v_pk_add_f32 v[10:11], v[18:19], 1.0 op_sel_hi:[1,0]
	v_pk_mul_f32 v[10:11], v[10:11], v[16:17]
	v_cvt_pk_fp8_f32 v8, v12, v13 op_sel:[0,0,1]
	v_cvt_pk_fp8_f32 v9, v10, v11 op_sel:[0,0,1]
	v_min_f32_e32 v11, v141, v6
	v_min_f32_e32 v10, v140, v6
	v_pk_mul_f32 v[12:13], v[10:11], s[84:85] op_sel_hi:[1,0]
	v_exp_f32_e32 v12, v12
	v_exp_f32_e32 v13, v13
	v_med3_f32 v15, v137, v7, v6
	v_pk_add_f32 v[12:13], v[12:13], 1.0 op_sel_hi:[1,0]
	v_med3_f32 v14, v136, v7, v6
	v_rcp_f32_e32 v12, v12
	v_rcp_f32_e32 v13, v13
	s_nop 0
	v_pk_mul_f32 v[10:11], v[10:11], v[12:13]
	v_pk_add_f32 v[12:13], v[14:15], 1.0 op_sel_hi:[1,0]
	v_pk_mul_f32 v[12:13], v[12:13], v[10:11]
	v_min_f32_e32 v11, v143, v6
	v_min_f32_e32 v10, v142, v6
	v_pk_mul_f32 v[14:15], v[10:11], s[84:85] op_sel_hi:[1,0]
	v_med3_f32 v17, v139, v7, v6
	v_exp_f32_e32 v14, v14
	v_exp_f32_e32 v15, v15
	v_med3_f32 v16, v138, v7, v6
	v_pk_add_f32 v[14:15], v[14:15], 1.0 op_sel_hi:[1,0]
	v_rcp_f32_e32 v14, v14
	v_rcp_f32_e32 v15, v15
	v_med3_f32 v19, v129, v7, v6
	v_med3_f32 v18, v128, v7, v6
	v_pk_mul_f32 v[10:11], v[10:11], v[14:15]
	v_pk_add_f32 v[14:15], v[16:17], 1.0 op_sel_hi:[1,0]
	s_nop 0
	v_pk_mul_f32 v[14:15], v[14:15], v[10:11]
	v_min_f32_e32 v11, v133, v6
	v_min_f32_e32 v10, v132, v6
	v_pk_mul_f32 v[16:17], v[10:11], s[84:85] op_sel_hi:[1,0]
	s_nop 0
	v_exp_f32_e32 v16, v16
	v_exp_f32_e32 v17, v17
	s_nop 0
	v_pk_add_f32 v[16:17], v[16:17], 1.0 op_sel_hi:[1,0]
	s_nop 0
	v_rcp_f32_e32 v16, v16
	v_rcp_f32_e32 v17, v17
	s_nop 0
	v_pk_mul_f32 v[10:11], v[10:11], v[16:17]
	v_pk_add_f32 v[16:17], v[18:19], 1.0 op_sel_hi:[1,0]
	s_nop 0
	v_pk_mul_f32 v[16:17], v[16:17], v[10:11]
	v_min_f32_e32 v11, v135, v6
	v_min_f32_e32 v10, v134, v6
	v_pk_mul_f32 v[18:19], v[10:11], s[84:85] op_sel_hi:[1,0]
	s_nop 0
	v_exp_f32_e32 v18, v18
	v_exp_f32_e32 v19, v19
	s_nop 0
	v_pk_add_f32 v[18:19], v[18:19], 1.0 op_sel_hi:[1,0]
	s_nop 0
	v_rcp_f32_e32 v18, v18
	v_rcp_f32_e32 v19, v19
	s_nop 0
	v_pk_mul_f32 v[18:19], v[10:11], v[18:19]
	v_cvt_pk_fp8_f32 v10, v12, v13
	v_cvt_pk_fp8_f32 v11, v16, v17
	v_pk_add_f32 v[12:13], v[20:21], 1.0 op_sel_hi:[1,0]
	v_pk_mul_f32 v[12:13], v[12:13], v[18:19]
	v_cvt_pk_fp8_f32 v10, v14, v15 op_sel:[0,0,1]
	v_cvt_pk_fp8_f32 v11, v12, v13 op_sel:[0,0,1]
	s_nop 0
	v_permlane16_swap_b32_e32 v8, v10
	s_nop 0
	v_permlane16_swap_b32_e32 v9, v11
	global_store_dwordx4 v[2:3], v[8:11], off
	v_min_f32_e32 v3, v125, v6
	v_min_f32_e32 v2, v124, v6
	v_pk_mul_f32 v[4:5], v[2:3], s[84:85] op_sel_hi:[1,0]
	v_exp_f32_e32 v4, v4
	v_exp_f32_e32 v5, v5
	s_nop 0
	v_pk_add_f32 v[4:5], v[4:5], 1.0 op_sel_hi:[1,0]
	v_med3_f32 v9, v121, v7, v6
	v_rcp_f32_e32 v4, v4
	v_rcp_f32_e32 v5, v5
	v_med3_f32 v8, v120, v7, v6
	v_pk_mul_f32 v[2:3], v[2:3], v[4:5]
	v_pk_add_f32 v[4:5], v[8:9], 1.0 op_sel_hi:[1,0]
	v_pk_mul_f32 v[4:5], v[4:5], v[2:3]
	v_min_f32_e32 v3, v127, v6
	v_min_f32_e32 v2, v126, v6
	v_pk_mul_f32 v[8:9], v[2:3], s[84:85] op_sel_hi:[1,0]
	v_exp_f32_e32 v8, v8
	v_exp_f32_e32 v9, v9
	v_med3_f32 v11, v123, v7, v6
	v_med3_f32 v10, v122, v7, v6
	v_pk_add_f32 v[8:9], v[8:9], 1.0 op_sel_hi:[1,0]
	v_rcp_f32_e32 v8, v8
	v_rcp_f32_e32 v9, v9
	v_med3_f32 v13, v113, v7, v6
	v_med3_f32 v12, v112, v7, v6
	v_pk_mul_f32 v[2:3], v[2:3], v[8:9]
	v_pk_add_f32 v[8:9], v[10:11], 1.0 op_sel_hi:[1,0]
	v_pk_mul_f32 v[8:9], v[8:9], v[2:3]
	v_min_f32_e32 v3, v117, v6
	v_min_f32_e32 v2, v116, v6
	v_pk_mul_f32 v[10:11], v[2:3], s[84:85] op_sel_hi:[1,0]
	v_exp_f32_e32 v10, v10
	v_exp_f32_e32 v11, v11
	v_med3_f32 v15, v115, v7, v6
	v_med3_f32 v14, v114, v7, v6
	v_pk_add_f32 v[10:11], v[10:11], 1.0 op_sel_hi:[1,0]
	v_rcp_f32_e32 v10, v10
	v_rcp_f32_e32 v11, v11
	v_med3_f32 v17, v99, v7, v6
	v_pk_mul_f32 v[2:3], v[2:3], v[10:11]
	v_pk_add_f32 v[10:11], v[12:13], 1.0 op_sel_hi:[1,0]
	v_med3_f32 v16, v98, v7, v6
	v_pk_mul_f32 v[10:11], v[10:11], v[2:3]
	v_min_f32_e32 v3, v119, v6
	v_min_f32_e32 v2, v118, v6
	v_pk_mul_f32 v[12:13], v[2:3], s[84:85] op_sel_hi:[1,0]
	s_nop 0
	v_exp_f32_e32 v12, v12
	v_exp_f32_e32 v13, v13
	s_nop 0
	v_pk_add_f32 v[12:13], v[12:13], 1.0 op_sel_hi:[1,0]
	s_nop 0
	v_rcp_f32_e32 v12, v12
	v_rcp_f32_e32 v13, v13
	s_nop 0
	v_pk_mul_f32 v[12:13], v[2:3], v[12:13]
	v_cvt_pk_fp8_f32 v3, v10, v11
	v_cvt_pk_fp8_f32 v2, v4, v5
	v_pk_add_f32 v[4:5], v[14:15], 1.0 op_sel_hi:[1,0]
	v_pk_mul_f32 v[4:5], v[4:5], v[12:13]
	v_cvt_pk_fp8_f32 v2, v8, v9 op_sel:[0,0,1]
	v_cvt_pk_fp8_f32 v3, v4, v5 op_sel:[0,0,1]
; DI float kf(float c) { asm volatile("" : "+v"(c)); return c; }
; DI unsigned pk_fp8x4(float a, float b, float c, float d) { int p = 0; p = __builtin_amdgcn_cvt_pk_fp8_f32(a, b, p, false); p = __builtin_amdgcn_cvt_pk_fp8_f32(c, d, p, true); return (unsigned)p; }
;     DI void operator()(const f32x4 (&acc)[2][2][4][2], const Unit& u, int wr, int wc, int fr, int fq) const {
;         const int row0 = u.pm * BM + wr * 64 + fr + (fq & 1) * 16; const int col0 = u.pn * HALF + wc * 32 + 8 * (fq & ~1); const float c7 = kf(7.f);
; #pragma unroll
;         for (int ai = 0; ai < 2; ++ai)
; #pragma unroll
;             for (int mp = 0; mp < 2; ++mp) { unsigned char* rowp = O + (size_t)(row0 + ai * HALF + mp * 32) * ldc + col0;
;                 u32x2 w[2];
; #pragma unroll
;                 for (int mm = 0; mm < 2; ++mm) { const int m = 2 * mp + mm; float o[8];
; #pragma unroll
;                     for (int n = 0; n < 2; ++n) { const f32x4 g = acc[ai][0][m][n], l = acc[ai][1][m][n];
; #pragma unroll
;                         for (int jp = 0; jp < 2; ++jp) {
;                             const f32x2 xg = __builtin_elementwise_min((f32x2){g[2 * jp], g[2 * jp + 1]}, (f32x2){c7, c7});
;                             const f32x2 xl = __builtin_elementwise_min(__builtin_elementwise_max((f32x2){l[2 * jp], l[2 * jp + 1]}, (f32x2){-c7, -c7}), (f32x2){c7, c7});
;                             const f32x2 z = xg * (-1.702f * 1.44269504f); f32x2 e; e.x = __builtin_amdgcn_exp2f(z.x); e.y = __builtin_amdgcn_exp2f(z.y);
;                             const f32x2 dn = e + 1.f; f32x2 rc; rc.x = __builtin_amdgcn_rcpf(dn.x); rc.y = __builtin_amdgcn_rcpf(dn.y);
;                             const f32x2 r2 = (xg * rc) * (xl + 1.f); o[n * 4 + 2 * jp] = r2.x; o[n * 4 + 2 * jp + 1] = r2.y; } }
;                     w[mm].x = pk_fp8x4(o[0], o[1], o[2], o[3]); w[mm].y = pk_fp8x4(o[4], o[5], o[6], o[7]); }
;                 const u32x2 sx = __builtin_amdgcn_permlane16_swap(w[0].x, w[1].x, false, false), sy = __builtin_amdgcn_permlane16_swap(w[0].y, w[1].y, false, false);
;                 *(u32x4*)rowp = (u32x4){sx.x, sy.x, sx.y, sy.y}; }
	v_min_f32_e32 v5, v109, v6
	v_min_f32_e32 v4, v108, v6
	v_pk_mul_f32 v[8:9], v[4:5], s[84:85] op_sel_hi:[1,0]
	v_exp_f32_e32 v8, v8
	v_exp_f32_e32 v9, v9
	v_med3_f32 v11, v105, v7, v6
	v_pk_add_f32 v[8:9], v[8:9], 1.0 op_sel_hi:[1,0]
	v_med3_f32 v10, v104, v7, v6
	v_rcp_f32_e32 v8, v8
	v_rcp_f32_e32 v9, v9
	s_nop 0
	v_pk_mul_f32 v[4:5], v[4:5], v[8:9]
	v_pk_add_f32 v[8:9], v[10:11], 1.0 op_sel_hi:[1,0]
	v_pk_mul_f32 v[8:9], v[8:9], v[4:5]
	v_min_f32_e32 v5, v111, v6
	v_min_f32_e32 v4, v110, v6
	v_pk_mul_f32 v[10:11], v[4:5], s[84:85] op_sel_hi:[1,0]
	v_med3_f32 v13, v107, v7, v6
	v_exp_f32_e32 v10, v10
	v_exp_f32_e32 v11, v11
	v_med3_f32 v12, v106, v7, v6
	v_pk_add_f32 v[10:11], v[10:11], 1.0 op_sel_hi:[1,0]
	v_rcp_f32_e32 v10, v10
	v_rcp_f32_e32 v11, v11
	v_med3_f32 v15, v97, v7, v6
	v_med3_f32 v14, v96, v7, v6
	v_pk_mul_f32 v[4:5], v[4:5], v[10:11]
	v_pk_add_f32 v[10:11], v[12:13], 1.0 op_sel_hi:[1,0]
	s_nop 0
	v_pk_mul_f32 v[10:11], v[10:11], v[4:5]
	v_min_f32_e32 v5, v101, v6
	v_min_f32_e32 v4, v100, v6
	v_pk_mul_f32 v[12:13], v[4:5], s[84:85] op_sel_hi:[1,0]
	s_nop 0
	v_exp_f32_e32 v12, v12
	v_exp_f32_e32 v13, v13
	s_nop 0
	v_pk_add_f32 v[12:13], v[12:13], 1.0 op_sel_hi:[1,0]
	s_nop 0
	v_rcp_f32_e32 v12, v12
	v_rcp_f32_e32 v13, v13
	s_nop 0
	v_pk_mul_f32 v[4:5], v[4:5], v[12:13]
	v_pk_add_f32 v[12:13], v[14:15], 1.0 op_sel_hi:[1,0]
	s_nop 0
	v_pk_mul_f32 v[12:13], v[12:13], v[4:5]
	v_min_f32_e32 v5, v103, v6
	v_min_f32_e32 v4, v102, v6
	v_pk_mul_f32 v[14:15], v[4:5], s[84:85] op_sel_hi:[1,0]
	s_nop 0
	v_exp_f32_e32 v14, v14
	v_exp_f32_e32 v15, v15
	s_nop 0
	v_pk_add_f32 v[14:15], v[14:15], 1.0 op_sel_hi:[1,0]
	s_nop 0
	v_rcp_f32_e32 v14, v14
	v_rcp_f32_e32 v15, v15
	s_nop 0
	v_pk_mul_f32 v[14:15], v[4:5], v[14:15]
	v_cvt_pk_fp8_f32 v4, v8, v9
	v_cvt_pk_fp8_f32 v5, v12, v13
	v_pk_add_f32 v[8:9], v[16:17], 1.0 op_sel_hi:[1,0]
	v_pk_mul_f32 v[8:9], v[8:9], v[14:15]
	v_cvt_pk_fp8_f32 v4, v10, v11 op_sel:[0,0,1]
	v_cvt_pk_fp8_f32 v5, v8, v9 op_sel:[0,0,1]
	v_add_co_u32_e32 v8, vcc, s2, v0
	v_permlane16_swap_b32_e32 v2, v4
	v_permlane16_swap_b32_e32 v3, v5
	v_addc_co_u32_e32 v9, vcc, 0, v1, vcc
	global_store_dwordx4 v[8:9], v[2:5], off
	s_nop 1
	v_min_f32_e32 v3, v93, v6
	v_min_f32_e32 v2, v92, v6
	v_pk_mul_f32 v[4:5], v[2:3], s[84:85] op_sel_hi:[1,0]
	v_exp_f32_e32 v4, v4
	v_exp_f32_e32 v5, v5
	v_med3_f32 v9, v89, v7, v6
	v_med3_f32 v8, v88, v7, v6
	v_pk_add_f32 v[4:5], v[4:5], 1.0 op_sel_hi:[1,0]
	v_rcp_f32_e32 v4, v4
	v_rcp_f32_e32 v5, v5
	s_nop 0
	v_pk_mul_f32 v[2:3], v[2:3], v[4:5]
	v_pk_add_f32 v[4:5], v[8:9], 1.0 op_sel_hi:[1,0]
	v_med3_f32 v11, v91, v7, v6
	v_pk_mul_f32 v[4:5], v[4:5], v[2:3]
	v_min_f32_e32 v3, v95, v6
	v_min_f32_e32 v2, v94, v6
	v_pk_mul_f32 v[8:9], v[2:3], s[84:85] op_sel_hi:[1,0]
	v_med3_f32 v10, v90, v7, v6
	v_exp_f32_e32 v8, v8
	v_exp_f32_e32 v9, v9
	s_nop 0
	v_pk_add_f32 v[8:9], v[8:9], 1.0 op_sel_hi:[1,0]
	v_med3_f32 v13, v81, v7, v6
	v_rcp_f32_e32 v8, v8
	v_rcp_f32_e32 v9, v9
	v_med3_f32 v12, v80, v7, v6
	v_pk_mul_f32 v[2:3], v[2:3], v[8:9]
	v_pk_add_f32 v[8:9], v[10:11], 1.0 op_sel_hi:[1,0]
	v_pk_mul_f32 v[8:9], v[8:9], v[2:3]
	v_min_f32_e32 v3, v85, v6
	v_min_f32_e32 v2, v84, v6
	v_pk_mul_f32 v[10:11], v[2:3], s[84:85] op_sel_hi:[1,0]
	v_exp_f32_e32 v10, v10
	v_exp_f32_e32 v11, v11
	v_med3_f32 v15, v83, v7, v6
	v_med3_f32 v14, v82, v7, v6
	v_pk_add_f32 v[10:11], v[10:11], 1.0 op_sel_hi:[1,0]
	v_rcp_f32_e32 v10, v10
	v_rcp_f32_e32 v11, v11
	v_max_f32_e32 v16, v66, v7
	v_add_co_u32_e32 v0, vcc, 0x28000, v0
	v_pk_mul_f32 v[2:3], v[2:3], v[10:11]
	v_pk_add_f32 v[10:11], v[12:13], 1.0 op_sel_hi:[1,0]
	v_addc_co_u32_e32 v1, vcc, 0, v1, vcc
	v_pk_mul_f32 v[10:11], v[10:11], v[2:3]
	v_min_f32_e32 v3, v87, v6
	v_min_f32_e32 v2, v86, v6
	v_pk_mul_f32 v[12:13], v[2:3], s[84:85] op_sel_hi:[1,0]
	s_andn2_b64 vcc, exec, s[36:37]
	v_exp_f32_e32 v12, v12
	v_exp_f32_e32 v13, v13
	s_nop 0
	v_pk_add_f32 v[12:13], v[12:13], 1.0 op_sel_hi:[1,0]
	s_nop 0
	v_rcp_f32_e32 v12, v12
	v_rcp_f32_e32 v13, v13
	s_nop 0
	v_pk_mul_f32 v[12:13], v[2:3], v[12:13]
	v_cvt_pk_fp8_f32 v3, v10, v11
	v_cvt_pk_fp8_f32 v2, v4, v5
	v_pk_add_f32 v[4:5], v[14:15], 1.0 op_sel_hi:[1,0]
	v_pk_mul_f32 v[4:5], v[4:5], v[12:13]
	v_cvt_pk_fp8_f32 v2, v8, v9 op_sel:[0,0,1]
	v_cvt_pk_fp8_f32 v3, v4, v5 op_sel:[0,0,1]
	v_min_f32_e32 v5, v77, v6
	v_min_f32_e32 v4, v76, v6
	v_pk_mul_f32 v[8:9], v[4:5], s[84:85] op_sel_hi:[1,0]
	v_exp_f32_e32 v8, v8
	v_exp_f32_e32 v9, v9
	v_med3_f32 v11, v73, v7, v6
	v_pk_add_f32 v[8:9], v[8:9], 1.0 op_sel_hi:[1,0]
	v_med3_f32 v10, v72, v7, v6
	v_rcp_f32_e32 v8, v8
	v_rcp_f32_e32 v9, v9
	s_nop 0
	v_pk_mul_f32 v[4:5], v[4:5], v[8:9]
	v_pk_add_f32 v[8:9], v[10:11], 1.0 op_sel_hi:[1,0]
	v_pk_mul_f32 v[8:9], v[8:9], v[4:5]
	v_min_f32_e32 v5, v79, v6
	v_min_f32_e32 v4, v78, v6
	v_pk_mul_f32 v[10:11], v[4:5], s[84:85] op_sel_hi:[1,0]
	v_med3_f32 v13, v75, v7, v6
	v_exp_f32_e32 v10, v10
	v_exp_f32_e32 v11, v11
	v_med3_f32 v12, v74, v7, v6
	v_pk_add_f32 v[10:11], v[10:11], 1.0 op_sel_hi:[1,0]
	v_rcp_f32_e32 v10, v10
	v_rcp_f32_e32 v11, v11
	v_med3_f32 v15, v65, v7, v6
	v_med3_f32 v14, v64, v7, v6
	v_pk_mul_f32 v[4:5], v[4:5], v[10:11]
	v_pk_add_f32 v[10:11], v[12:13], 1.0 op_sel_hi:[1,0]
	v_max_f32_e32 v7, v67, v7
	v_pk_mul_f32 v[10:11], v[10:11], v[4:5]
	v_min_f32_e32 v5, v69, v6
	v_min_f32_e32 v4, v68, v6
	v_pk_mul_f32 v[12:13], v[4:5], s[84:85] op_sel_hi:[1,0]
	v_min_f32_e32 v7, v7, v6
	v_exp_f32_e32 v12, v12
	v_exp_f32_e32 v13, v13
	s_nop 0
	v_pk_add_f32 v[12:13], v[12:13], 1.0 op_sel_hi:[1,0]
	s_nop 0
	v_rcp_f32_e32 v12, v12
	v_rcp_f32_e32 v13, v13
	s_nop 0
	v_pk_mul_f32 v[4:5], v[4:5], v[12:13]
	v_pk_add_f32 v[12:13], v[14:15], 1.0 op_sel_hi:[1,0]
	s_nop 0
	v_pk_mul_f32 v[12:13], v[12:13], v[4:5]
	v_min_f32_e32 v5, v71, v6
	v_min_f32_e32 v4, v70, v6
	v_pk_mul_f32 v[14:15], v[4:5], s[84:85] op_sel_hi:[1,0]
	v_min_f32_e32 v6, v16, v6
	v_exp_f32_e32 v14, v14
	v_exp_f32_e32 v15, v15
	v_pk_add_f32 v[6:7], v[6:7], 1.0 op_sel_hi:[1,0]
	v_pk_add_f32 v[14:15], v[14:15], 1.0 op_sel_hi:[1,0]
	s_nop 0
	v_rcp_f32_e32 v14, v14
	v_rcp_f32_e32 v15, v15
	s_nop 0
	v_pk_mul_f32 v[14:15], v[4:5], v[14:15]
	v_cvt_pk_fp8_f32 v4, v8, v9
	v_cvt_pk_fp8_f32 v5, v12, v13
	v_pk_mul_f32 v[6:7], v[6:7], v[14:15]
	v_cvt_pk_fp8_f32 v4, v10, v11 op_sel:[0,0,1]
	v_cvt_pk_fp8_f32 v5, v6, v7 op_sel:[0,0,1]
	s_nop 0
	v_permlane16_swap_b32_e32 v2, v4
	v_permlane16_swap_b32_e32 v3, v5
	global_store_dwordx4 v[0:1], v[2:5], off
	s_cbranch_vccnz .LBB0_1178
	v_add_u32_e32 v0, s6, v232
	ds_read_b128 v[76:79], v0 offset:1024
	ds_read_b128 v[68:71], v0 offset:1040
	ds_read_b128 v[72:75], v0 offset:1536
	ds_read_b128 v[64:67], v0 offset:1552
	s_andn2_b64 vcc, exec, s[44:45]
	s_cbranch_vccnz .LBB0_1177
	s_barrier
	s_branch .LBB0_1177

; DI float kf(float c) { asm volatile("" : "+v"(c)); return c; }
; DI unsigned pk_fp8x4(float a, float b, float c, float d) { int p = 0; p = __builtin_amdgcn_cvt_pk_fp8_f32(a, b, p, false); p = __builtin_amdgcn_cvt_pk_fp8_f32(c, d, p, true); return (unsigned)p; }
;     DI void operator()(const f32x4 (&acc)[2][2][4][2], const Unit& u, int wr, int wc, int fr, int fq) const {
;         const int row0 = u.pm * BM + wr * 64 + fr; const int col0 = u.pn * BM + wc * 32 + 8 * (fq & ~1) + (fq & 1) * HALF; const float cmax = kf(448.f);
; #pragma unroll
;         for (int ai = 0; ai < 2; ++ai)
; #pragma unroll
;             for (int m = 0; m < 4; ++m) { unsigned char* rowp = O + (size_t)(row0 + ai * HALF + m * 16) * ldc + col0;
;                 u32x2 w[2];
; #pragma unroll
;                 for (int bj = 0; bj < 2; ++bj) { f32x4 v0 = acc[ai][bj][m][0], v1 = acc[ai][bj][m][1];
; #pragma unroll
;                     for (int i = 0; i < 4; ++i) { v0[i] = __builtin_amdgcn_fmed3f(v0[i], -cmax, cmax); v1[i] = __builtin_amdgcn_fmed3f(v1[i], -cmax, cmax); }
;                     w[bj].x = pk_fp8x4(v0[0], v0[1], v0[2], v0[3]); w[bj].y = pk_fp8x4(v1[0], v1[1], v1[2], v1[3]); }
;                 const u32x2 sx = __builtin_amdgcn_permlane16_swap(w[0].x, w[1].x, false, false), sy = __builtin_amdgcn_permlane16_swap(w[0].y, w[1].y, false, false);
;                 *(u32x4*)rowp = (u32x4){sx.x, sy.x, sx.y, sy.y}; }
;     }
.LBB0_1327:
	s_lshl_b32 s2, s82, 8
	v_mbcnt_lo_u32_b32 v0, -1, 0
	v_mbcnt_hi_u32_b32 v0, -1, v0
	s_add_i32 s2, s2, s81
	v_ashrrev_i32_e32 v1, 4, v0
	v_and_or_b32 v4, v0, 15, s2
	s_lshl_b32 s2, s10, 8
	v_lshlrev_b32_e32 v0, 3, v1
	v_lshlrev_b32_e32 v1, 7, v1
	s_or_b32 s2, s2, s70
	v_and_b32_e32 v0, -16, v0
	v_and_b32_e32 v1, 0x80, v1
	v_mov_b32_e32 v6, 0x43e00000
	v_ashrrev_i32_e32 v5, 31, v4
	v_add3_u32 v2, s2, v0, v1
	v_lshlrev_b64 v[0:1], 10, v[4:5]
	v_med3_f32 v5, v188, -v6, v6
	v_med3_f32 v9, v189, -v6, v6
	v_med3_f32 v7, v184, -v6, v6
	v_med3_f32 v10, v185, -v6, v6
	v_cvt_pk_fp8_f32 v8, v5, v9
	v_cvt_pk_fp8_f32 v9, v7, v10
	v_med3_f32 v11, v190, -v6, v6
	v_med3_f32 v13, v191, -v6, v6
	v_med3_f32 v12, v186, -v6, v6
	v_med3_f32 v14, v187, -v6, v6
	v_cvt_pk_fp8_f32 v8, v11, v13 op_sel:[0,0,1]
	v_med3_f32 v5, v180, -v6, v6
	v_med3_f32 v11, v181, -v6, v6
	v_cvt_pk_fp8_f32 v9, v12, v14 op_sel:[0,0,1]
	v_med3_f32 v7, v176, -v6, v6
	v_med3_f32 v12, v177, -v6, v6
	v_cvt_pk_fp8_f32 v10, v5, v11
	v_cvt_pk_fp8_f32 v11, v7, v12
	v_med3_f32 v13, v182, -v6, v6
	v_med3_f32 v14, v178, -v6, v6
	v_med3_f32 v15, v183, -v6, v6
	v_med3_f32 v16, v179, -v6, v6
	v_cvt_pk_fp8_f32 v10, v13, v15 op_sel:[0,0,1]
	v_cvt_pk_fp8_f32 v11, v14, v16 op_sel:[0,0,1]
	v_ashrrev_i32_e32 v3, 31, v2
	v_lshl_add_u64 v[0:1], s[46:47], 0, v[0:1]
	v_lshl_add_u64 v[0:1], v[0:1], 0, v[2:3]
	v_permlane16_swap_b32_e32 v8, v10
	v_permlane16_swap_b32_e32 v9, v11
	global_store_dwordx4 v[0:1], v[8:11], off
	v_med3_f32 v5, v172, -v6, v6
	v_med3_f32 v7, v168, -v6, v6
	v_or_b32_e32 v8, 16, v4
	v_ashrrev_i32_e32 v9, 31, v8
	v_lshlrev_b64 v[8:9], 10, v[8:9]
	v_lshl_add_u64 v[12:13], s[46:47], 0, v[8:9]
	v_med3_f32 v9, v173, -v6, v6
	v_med3_f32 v10, v169, -v6, v6
	v_cvt_pk_fp8_f32 v8, v5, v9
	v_cvt_pk_fp8_f32 v9, v7, v10
	v_med3_f32 v11, v174, -v6, v6
	v_med3_f32 v15, v175, -v6, v6
	v_med3_f32 v14, v170, -v6, v6
	v_med3_f32 v16, v171, -v6, v6
	v_cvt_pk_fp8_f32 v8, v11, v15 op_sel:[0,0,1]
	v_med3_f32 v5, v164, -v6, v6
	v_med3_f32 v11, v165, -v6, v6
	v_cvt_pk_fp8_f32 v9, v14, v16 op_sel:[0,0,1]
	v_med3_f32 v7, v160, -v6, v6
	v_med3_f32 v14, v161, -v6, v6
	v_cvt_pk_fp8_f32 v10, v5, v11
	v_cvt_pk_fp8_f32 v11, v7, v14
	v_med3_f32 v15, v166, -v6, v6
	v_med3_f32 v16, v162, -v6, v6
	v_med3_f32 v17, v167, -v6, v6
	v_med3_f32 v18, v163, -v6, v6
	v_cvt_pk_fp8_f32 v10, v15, v17 op_sel:[0,0,1]
	v_cvt_pk_fp8_f32 v11, v16, v18 op_sel:[0,0,1]
	v_lshl_add_u64 v[12:13], v[12:13], 0, v[2:3]
	v_med3_f32 v5, v156, -v6, v6
	v_permlane16_swap_b32_e32 v8, v10
	v_permlane16_swap_b32_e32 v9, v11
	global_store_dwordx4 v[12:13], v[8:11], off
	v_med3_f32 v7, v152, -v6, v6
	v_med3_f32 v15, v159, -v6, v6
	v_or_b32_e32 v8, 32, v4
	v_ashrrev_i32_e32 v9, 31, v8
	v_lshlrev_b64 v[8:9], 10, v[8:9]
	v_lshl_add_u64 v[12:13], s[46:47], 0, v[8:9]
	v_med3_f32 v9, v157, -v6, v6
	v_med3_f32 v10, v153, -v6, v6
	v_cvt_pk_fp8_f32 v8, v5, v9
	v_cvt_pk_fp8_f32 v9, v7, v10
	v_med3_f32 v11, v158, -v6, v6
	v_med3_f32 v14, v154, -v6, v6
	v_med3_f32 v16, v155, -v6, v6
	v_cvt_pk_fp8_f32 v8, v11, v15 op_sel:[0,0,1]
	v_med3_f32 v5, v148, -v6, v6
	v_med3_f32 v11, v149, -v6, v6
	v_cvt_pk_fp8_f32 v9, v14, v16 op_sel:[0,0,1]
	v_med3_f32 v7, v144, -v6, v6
	v_med3_f32 v14, v145, -v6, v6
	v_cvt_pk_fp8_f32 v10, v5, v11
	v_cvt_pk_fp8_f32 v11, v7, v14
	v_med3_f32 v15, v150, -v6, v6
	v_med3_f32 v16, v146, -v6, v6
	v_med3_f32 v17, v151, -v6, v6
	v_med3_f32 v18, v147, -v6, v6
	v_cvt_pk_fp8_f32 v10, v15, v17 op_sel:[0,0,1]
	v_cvt_pk_fp8_f32 v11, v16, v18 op_sel:[0,0,1]
	v_lshl_add_u64 v[12:13], v[12:13], 0, v[2:3]
	v_med3_f32 v7, v140, -v6, v6
	v_permlane16_swap_b32_e32 v8, v10
	v_permlane16_swap_b32_e32 v9, v11
	global_store_dwordx4 v[12:13], v[8:11], off
	v_med3_f32 v12, v142, -v6, v6
	v_med3_f32 v13, v138, -v6, v6
	v_med3_f32 v9, v141, -v6, v6
	v_med3_f32 v10, v136, -v6, v6
	v_med3_f32 v11, v137, -v6, v6
	v_cvt_pk_fp8_f32 v8, v7, v9
	v_cvt_pk_fp8_f32 v9, v10, v11
	v_med3_f32 v14, v143, -v6, v6
	v_med3_f32 v15, v139, -v6, v6
	v_med3_f32 v7, v132, -v6, v6
	v_med3_f32 v11, v133, -v6, v6
	v_cvt_pk_fp8_f32 v8, v12, v14 op_sel:[0,0,1]
	v_cvt_pk_fp8_f32 v9, v13, v15 op_sel:[0,0,1]
	v_med3_f32 v12, v128, -v6, v6
	v_med3_f32 v13, v129, -v6, v6
	v_cvt_pk_fp8_f32 v10, v7, v11
	v_cvt_pk_fp8_f32 v11, v12, v13
	v_med3_f32 v14, v134, -v6, v6
	v_med3_f32 v15, v130, -v6, v6
	v_med3_f32 v16, v135, -v6, v6
	v_med3_f32 v17, v131, -v6, v6
	v_or_b32_e32 v4, 48, v4
	v_cvt_pk_fp8_f32 v10, v14, v16 op_sel:[0,0,1]
	v_cvt_pk_fp8_f32 v11, v15, v17 op_sel:[0,0,1]
	v_ashrrev_i32_e32 v5, 31, v4
; DI float kf(float c) { asm volatile("" : "+v"(c)); return c; }
; DI unsigned pk_fp8x4(float a, float b, float c, float d) { int p = 0; p = __builtin_amdgcn_cvt_pk_fp8_f32(a, b, p, false); p = __builtin_amdgcn_cvt_pk_fp8_f32(c, d, p, true); return (unsigned)p; }
;     DI void operator()(const f32x4 (&acc)[2][2][4][2], const Unit& u, int wr, int wc, int fr, int fq) const {
;         const int row0 = u.pm * BM + wr * 64 + fr; const int col0 = u.pn * BM + wc * 32 + 8 * (fq & ~1) + (fq & 1) * HALF; const float cmax = kf(448.f);
; #pragma unroll
;         for (int ai = 0; ai < 2; ++ai)
; #pragma unroll
;             for (int m = 0; m < 4; ++m) { unsigned char* rowp = O + (size_t)(row0 + ai * HALF + m * 16) * ldc + col0;
;                 u32x2 w[2];
; #pragma unroll
;                 for (int bj = 0; bj < 2; ++bj) { f32x4 v0 = acc[ai][bj][m][0], v1 = acc[ai][bj][m][1];
; #pragma unroll
;                     for (int i = 0; i < 4; ++i) { v0[i] = __builtin_amdgcn_fmed3f(v0[i], -cmax, cmax); v1[i] = __builtin_amdgcn_fmed3f(v1[i], -cmax, cmax); }
;                     w[bj].x = pk_fp8x4(v0[0], v0[1], v0[2], v0[3]); w[bj].y = pk_fp8x4(v1[0], v1[1], v1[2], v1[3]); }
;                 const u32x2 sx = __builtin_amdgcn_permlane16_swap(w[0].x, w[1].x, false, false), sy = __builtin_amdgcn_permlane16_swap(w[0].y, w[1].y, false, false);
;                 *(u32x4*)rowp = (u32x4){sx.x, sy.x, sx.y, sy.y}; }
;     }
	v_lshlrev_b64 v[4:5], 10, v[4:5]
	v_lshl_add_u64 v[4:5], s[46:47], 0, v[4:5]
	v_lshl_add_u64 v[2:3], v[4:5], 0, v[2:3]
	v_permlane16_swap_b32_e32 v8, v10
	v_permlane16_swap_b32_e32 v9, v11
	global_store_dwordx4 v[2:3], v[8:11], off
	v_med3_f32 v3, v124, -v6, v6
	v_med3_f32 v5, v125, -v6, v6
	v_med3_f32 v4, v120, -v6, v6
	v_med3_f32 v7, v121, -v6, v6
	v_cvt_pk_fp8_f32 v2, v3, v5
	v_cvt_pk_fp8_f32 v3, v4, v7
	v_med3_f32 v8, v126, -v6, v6
	v_med3_f32 v10, v127, -v6, v6
	v_med3_f32 v9, v122, -v6, v6
	v_med3_f32 v11, v123, -v6, v6
	v_cvt_pk_fp8_f32 v2, v8, v10 op_sel:[0,0,1]
	v_med3_f32 v5, v116, -v6, v6
	v_med3_f32 v8, v117, -v6, v6
	v_cvt_pk_fp8_f32 v3, v9, v11 op_sel:[0,0,1]
	v_med3_f32 v7, v112, -v6, v6
	v_med3_f32 v9, v113, -v6, v6
	v_cvt_pk_fp8_f32 v4, v5, v8
	v_cvt_pk_fp8_f32 v5, v7, v9
	v_med3_f32 v10, v118, -v6, v6
	v_med3_f32 v11, v114, -v6, v6
	v_med3_f32 v12, v119, -v6, v6
	v_med3_f32 v13, v115, -v6, v6
	v_cvt_pk_fp8_f32 v4, v10, v12 op_sel:[0,0,1]
	v_cvt_pk_fp8_f32 v5, v11, v13 op_sel:[0,0,1]
	s_mov_b32 s2, 0x20000
	v_add_co_u32_e32 v8, vcc, s2, v0
	v_permlane16_swap_b32_e32 v2, v4
	v_permlane16_swap_b32_e32 v3, v5
	v_addc_co_u32_e32 v9, vcc, 0, v1, vcc
	global_store_dwordx4 v[8:9], v[2:5], off
	v_med3_f32 v7, v105, -v6, v6
	v_med3_f32 v8, v110, -v6, v6
	v_med3_f32 v3, v108, -v6, v6
	v_med3_f32 v5, v109, -v6, v6
	v_med3_f32 v4, v104, -v6, v6
	v_cvt_pk_fp8_f32 v2, v3, v5
	v_cvt_pk_fp8_f32 v3, v4, v7
	v_med3_f32 v10, v111, -v6, v6
	v_med3_f32 v9, v106, -v6, v6
	v_med3_f32 v11, v107, -v6, v6
	v_cvt_pk_fp8_f32 v2, v8, v10 op_sel:[0,0,1]
	v_med3_f32 v5, v100, -v6, v6
	v_med3_f32 v8, v101, -v6, v6
	v_cvt_pk_fp8_f32 v3, v9, v11 op_sel:[0,0,1]
	v_med3_f32 v7, v96, -v6, v6
	v_med3_f32 v9, v97, -v6, v6
	v_cvt_pk_fp8_f32 v4, v5, v8
	v_cvt_pk_fp8_f32 v5, v7, v9
	v_med3_f32 v10, v102, -v6, v6
	v_med3_f32 v11, v98, -v6, v6
	v_med3_f32 v12, v103, -v6, v6
	v_med3_f32 v13, v99, -v6, v6
	v_cvt_pk_fp8_f32 v4, v10, v12 op_sel:[0,0,1]
	v_cvt_pk_fp8_f32 v5, v11, v13 op_sel:[0,0,1]
	s_mov_b32 s2, 0x24000
	v_add_co_u32_e32 v8, vcc, s2, v0
	v_permlane16_swap_b32_e32 v2, v4
	v_permlane16_swap_b32_e32 v3, v5
	v_addc_co_u32_e32 v9, vcc, 0, v1, vcc
	global_store_dwordx4 v[8:9], v[2:5], off
	v_med3_f32 v7, v89, -v6, v6
	v_med3_f32 v8, v94, -v6, v6
	v_med3_f32 v3, v92, -v6, v6
	v_med3_f32 v5, v93, -v6, v6
	v_med3_f32 v4, v88, -v6, v6
	v_cvt_pk_fp8_f32 v2, v3, v5
	v_cvt_pk_fp8_f32 v3, v4, v7
	v_med3_f32 v10, v95, -v6, v6
	v_med3_f32 v9, v90, -v6, v6
	v_med3_f32 v11, v91, -v6, v6
	v_cvt_pk_fp8_f32 v2, v8, v10 op_sel:[0,0,1]
	v_med3_f32 v5, v84, -v6, v6
	v_med3_f32 v8, v85, -v6, v6
	v_cvt_pk_fp8_f32 v3, v9, v11 op_sel:[0,0,1]
	v_med3_f32 v7, v80, -v6, v6
	v_med3_f32 v9, v81, -v6, v6
	v_cvt_pk_fp8_f32 v4, v5, v8
	v_cvt_pk_fp8_f32 v5, v7, v9
	v_med3_f32 v10, v86, -v6, v6
	v_med3_f32 v11, v82, -v6, v6
	v_med3_f32 v12, v87, -v6, v6
	v_med3_f32 v13, v83, -v6, v6
	v_cvt_pk_fp8_f32 v4, v10, v12 op_sel:[0,0,1]
	v_cvt_pk_fp8_f32 v5, v11, v13 op_sel:[0,0,1]
	s_mov_b32 s2, 0x28000
	v_add_co_u32_e32 v8, vcc, s2, v0
	v_permlane16_swap_b32_e32 v2, v4
	v_permlane16_swap_b32_e32 v3, v5
	v_addc_co_u32_e32 v9, vcc, 0, v1, vcc
	global_store_dwordx4 v[8:9], v[2:5], off
	v_med3_f32 v7, v77, -v6, v6
	v_med3_f32 v8, v74, -v6, v6
	v_med3_f32 v3, v72, -v6, v6
	v_med3_f32 v5, v73, -v6, v6
	v_med3_f32 v4, v76, -v6, v6
	v_cvt_pk_fp8_f32 v2, v3, v5
	v_cvt_pk_fp8_f32 v3, v4, v7
	v_med3_f32 v10, v75, -v6, v6
	v_med3_f32 v9, v78, -v6, v6
	v_med3_f32 v11, v79, -v6, v6
	v_cvt_pk_fp8_f32 v2, v8, v10 op_sel:[0,0,1]
	v_med3_f32 v5, v64, -v6, v6
	v_med3_f32 v8, v65, -v6, v6
	v_cvt_pk_fp8_f32 v3, v9, v11 op_sel:[0,0,1]
	v_med3_f32 v7, v68, -v6, v6
	v_med3_f32 v9, v69, -v6, v6
	v_cvt_pk_fp8_f32 v4, v5, v8
	v_cvt_pk_fp8_f32 v5, v7, v9
	v_med3_f32 v10, v66, -v6, v6
	v_med3_f32 v11, v70, -v6, v6
	v_med3_f32 v12, v67, -v6, v6
	v_med3_f32 v6, v71, -v6, v6
	v_cvt_pk_fp8_f32 v4, v10, v12 op_sel:[0,0,1]
	v_cvt_pk_fp8_f32 v5, v11, v6 op_sel:[0,0,1]
	v_add_co_u32_e32 v0, vcc, 0x2c000, v0
	v_permlane16_swap_b32_e32 v2, v4
	s_nop 0
	v_addc_co_u32_e32 v1, vcc, 0, v1, vcc
	v_permlane16_swap_b32_e32 v3, v5
	s_mov_b64 s[4:5], -1
	s_andn2_b64 vcc, exec, s[36:37]
	global_store_dwordx4 v[0:1], v[2:5], off
	s_cbranch_vccnz .LBB0_1311
	v_add_u32_e32 v0, s6, v235
	ds_read_b128 v[12:15], v0 offset:1024
	ds_read_b128 v[8:11], v0 offset:1040
	ds_read_b128 v[4:7], v0 offset:1536
	ds_read_b128 v[0:3], v0 offset:1552
	s_andn2_b64 vcc, exec, s[44:45]
	s_cbranch_vccnz .LBB0_1310
	s_barrier
	s_branch .LBB0_1310

; DI void phase_combine(const Frame& F, int l) {
;     ...
;     for (int blk = F.gw; blk < T / 16; blk += F.NGW) {
;         const int t0 = blk * 16, b = t0 / SEQ; const float* m = MOD + ((size_t)l * NB + b) * 6144;
;         f32x4 Bv[4], Av[4], Sv[4];
;         { f32x4 g[4], c[4]; load_vec(F.ap->in[7] + (size_t)l * D, F.lane, g); load_vec(m + 5 * D, F.lane, c);
; #pragma unroll
;           for (int j = 0; j < 4; ++j) { Bv[j] = g[j] * c[j]; Av[j] = Bv[j]; Sv[j] = Bv[j]; }
;           if (more) { const float* m2 = MOD + ((size_t)(l + 1) * NB + b) * 6144; load_vec(F.ap->in[4] + (size_t)(l + 1) * D, F.lane, g); load_vec(m2 + 1 * D, F.lane, c); load_vec(m2, F.lane, Sv);
; #pragma unroll
;               for (int j = 0; j < 4; ++j) Av[j] = g[j] * (c[j] + 1.f); } }
;         const int ev = tok_e[(size_t)t0 * 4 + F.lane]; const int slotv = pstart[ev] + tok_p[(size_t)t0 * 4 + F.lane]; const int gvi = __builtin_bit_cast(int, tok_g[(size_t)t0 * 4 + F.lane]);
.LBB0_1387:
	s_ashr_i32 s2, s6, 31
	s_lshr_b32 s2, s2, 24
	s_add_i32 s2, s6, s2
	s_ashr_i32 s2, s2, 8
	s_ashr_i32 s4, s2, 31
	s_add_u32 s5, s48, s2
	s_addc_u32 s10, s49, s4
	s_mulk_i32 s10, 0x6000
	s_mul_hi_u32 s12, s5, 0x6000
	s_add_i32 s12, s12, s10
	s_mulk_i32 s5, 0x6000
	s_add_u32 s5, s8, s5
	s_addc_u32 s10, s9, s12
	s_add_u32 s12, s5, 0x5000
	s_addc_u32 s13, s10, 0
	v_lshlrev_b32_e32 v97, 2, v192
	s_lshl_b32 s24, s6, 4
	s_ashr_i32 s25, s24, 31
	s_lshl_b64 s[24:25], s[24:25], 4
	v_lshl_or_b32 v114, v64, 2, s24
	v_mov_b32_e32 v115, s25
	v_lshl_add_u64 v[116:117], s[40:41], 0, v[114:115]
	global_load_dword v112, v[116:117], off
	v_lshl_add_u64 v[116:117], s[42:43], 0, v[114:115]
	global_load_dword v113, v[116:117], off
	v_lshl_add_u64 v[116:117], s[44:45], 0, v[114:115]
	global_load_dword v98, v[116:117], off
	global_load_dwordx4 v[0:3], v97, s[12:13]
	global_load_dwordx4 v[4:7], v[66:67], off
	global_load_dwordx4 v[8:11], v[66:67], off offset:16
	global_load_dwordx4 v[12:15], v97, s[12:13] offset:16
	global_load_dwordx4 v[16:19], v96, s[12:13]
	global_load_dwordx4 v[20:23], v[66:67], off offset:2048
	global_load_dwordx4 v[24:27], v[66:67], off offset:2064
	global_load_dwordx4 v[28:31], v96, s[12:13] offset:16
	v_cndmask_b32_e64 v32, 0, 1, s[46:47]
	v_cmp_ne_u32_e64 s[36:37], 1, v32
	s_andn2_b64 vcc, exec, s[46:47]
	s_waitcnt vmcnt(0)
	v_pk_mul_f32 v[2:3], v[6:7], v[2:3]
	v_pk_mul_f32 v[0:1], v[4:5], v[0:1]
	v_pk_mul_f32 v[6:7], v[10:11], v[14:15]
	v_pk_mul_f32 v[4:5], v[8:9], v[12:13]
	v_pk_mul_f32 v[10:11], v[22:23], v[18:19]
	v_pk_mul_f32 v[8:9], v[20:21], v[16:17]
	v_pk_mul_f32 v[14:15], v[26:27], v[30:31]
	v_pk_mul_f32 v[12:13], v[24:25], v[28:29]
	v_mov_b64_e32 v[42:43], v[10:11]
	v_mov_b64_e32 v[46:47], v[14:15]
	v_mov_b64_e32 v[38:39], v[6:7]
	v_mov_b64_e32 v[34:35], v[2:3]
	v_mov_b64_e32 v[26:27], v[14:15]
	v_mov_b64_e32 v[30:31], v[10:11]
	v_mov_b64_e32 v[18:19], v[6:7]
	v_mov_b64_e32 v[22:23], v[2:3]
	v_mov_b64_e32 v[44:45], v[12:13]
	v_mov_b64_e32 v[40:41], v[8:9]
	v_mov_b64_e32 v[36:37], v[4:5]
	v_mov_b64_e32 v[32:33], v[0:1]
	v_mov_b64_e32 v[24:25], v[12:13]
	v_mov_b64_e32 v[28:29], v[8:9]
	v_mov_b64_e32 v[16:17], v[4:5]
	v_mov_b64_e32 v[20:21], v[0:1]
	s_cbranch_vccnz .LBB0_1389
	s_add_u32 s2, s50, s2
	s_addc_u32 s4, s51, s4
	s_load_dwordx2 s[12:13], s[38:39], 0x20
	s_mulk_i32 s4, 0x6000
	s_mul_hi_u32 s5, s2, 0x6000
	s_add_i32 s5, s5, s4
	s_mulk_i32 s2, 0x6000
	s_add_u32 s4, s8, s2
	s_addc_u32 s5, s9, s5
	s_waitcnt lgkmcnt(0)
	s_add_u32 s12, s12, s52
	s_addc_u32 s13, s13, s53
	global_load_dwordx4 v[36:39], v97, s[12:13] offset:16
	global_load_dwordx4 v[32:35], v97, s[12:13]
	global_load_dwordx4 v[44:47], v97, s[12:13] offset:2064
	global_load_dwordx4 v[40:43], v97, s[12:13] offset:2048
	s_add_u32 s12, s4, 0x1000
	s_addc_u32 s13, s5, 0
	global_load_dwordx4 v[48:51], v97, s[12:13] offset:16
	global_load_dwordx4 v[52:55], v97, s[12:13]
	global_load_dwordx4 v[56:59], v96, s[12:13] offset:16
	global_load_dwordx4 v[60:63], v96, s[12:13]
	global_load_dwordx4 v[16:19], v97, s[4:5] offset:16
	global_load_dwordx4 v[20:23], v97, s[4:5]
	global_load_dwordx4 v[24:27], v97, s[4:5] offset:2064
	global_load_dwordx4 v[28:31], v97, s[4:5] offset:2048
	s_waitcnt vmcnt(7)
	v_pk_add_f32 v[50:51], v[50:51], 1.0 op_sel_hi:[1,0]
	v_pk_add_f32 v[48:49], v[48:49], 1.0 op_sel_hi:[1,0]
	v_pk_mul_f32 v[38:39], v[38:39], v[50:51]
	v_pk_mul_f32 v[36:37], v[36:37], v[48:49]
	s_waitcnt vmcnt(4)
	v_pk_add_f32 v[48:49], v[62:63], 1.0 op_sel_hi:[1,0]
	v_pk_add_f32 v[50:51], v[60:61], 1.0 op_sel_hi:[1,0]
	v_pk_add_f32 v[54:55], v[54:55], 1.0 op_sel_hi:[1,0]
	v_pk_add_f32 v[52:53], v[52:53], 1.0 op_sel_hi:[1,0]
	v_pk_mul_f32 v[42:43], v[42:43], v[48:49]
	v_pk_mul_f32 v[40:41], v[40:41], v[50:51]
	v_pk_add_f32 v[48:49], v[58:59], 1.0 op_sel_hi:[1,0]
	v_pk_add_f32 v[50:51], v[56:57], 1.0 op_sel_hi:[1,0]
	v_pk_mul_f32 v[34:35], v[34:35], v[54:55]
	v_pk_mul_f32 v[32:33], v[32:33], v[52:53]
	v_pk_mul_f32 v[46:47], v[46:47], v[48:49]
	v_pk_mul_f32 v[44:45], v[44:45], v[50:51]
.LBB0_1389:
	s_mov_b32 s22, 7
	s_mov_b32 s54, s17
	v_lshl_add_u32 v48, v112, 2, 0
	v_add_u32_e32 v48, 0x20200, v48
	ds_read_b32 v48, v48
	s_waitcnt lgkmcnt(0)
	v_add_u32_e32 v99, v113, v48
	s_branch .LBB0_1391
